# expert-choice top-k latent sets: the 16 key loads per lane issued together (was 8 x load-pair + vmcnt(0)); radix histogram pass reads its 16 keys from LDS up front with counted lgkmcnt waits
# baseline (speedup 1.0000x reference)
; __device__ __forceinline__ void topk_phase(Frame& F, KArgs a, int nsets) {
;     ...
;     for (int sidx = blockIdx.x; sidx < nsets; sidx += F.G) {
;         const bool lat = sidx < 128; const int k = lat ? sidx : sidx - 128, b = k >> 4, e = k & 15;
;         const int row0 = b * TPS + (lat ? 0 : SEQ), n = lat ? SEQ : CTXL, cap = lat ? CAP_L : CAP_C;
;         const int pairbase = lat ? (b * 16 + e) * CAP_L : NPAIR_L + e * (NB * CAP_C) + b * CAP_C;
;         for (int i = tid; i < n; i += 512) keys[i] = __float_as_uint(AFF[(size_t)(row0 + i) * 16 + e]);
.LBB0_1273:
	s_and_b64 s[24:25], s[28:29], exec
	s_mulk_i32 s26, 0x2100
	s_cselect_b32 s24, 0, 0x2000
	s_add_i32 s85, s26, s24
	s_and_b64 s[24:25], s[28:29], exec
	s_movk_i32 s24, 0x2000
	s_cselect_b32 s86, s24, 0x100
	v_cmp_gt_i32_e32 vcc, s86, v202
	s_and_saveexec_b64 s[30:31], vcc
	s_cbranch_execz .LBB0_1285
	s_lshl_b32 s24, s87, 2
	v_max_i32_e32 v2, s86, v203
	s_add_u32 s48, s68, s24
	v_add_u32_e32 v4, v2, v21
	s_movk_i32 s24, 0x2600
	v_cmp_gt_u32_e64 s[52:53], s24, v4
	s_movk_i32 s24, 0x25ff
	s_addc_u32 s49, s69, 0
	v_cmp_lt_u32_e64 s[26:27], s24, v4
	v_mov_b32_e32 v2, v202
	v_mov_b32_e32 v3, v1
	s_and_saveexec_b64 s[58:59], s[26:27]
	s_cbranch_execz .LBB0_1282
	v_and_b32_e32 v2, 0xfffffe00, v4
	v_add_u32_e32 v3, s85, v202
	v_add_u32_e32 v2, v3, v2
	v_cmp_ge_i32_e64 s[26:27], v2, v3
	s_mov_b64 s[24:25], -1
	v_mov_b32_e32 v2, v202
	v_mov_b32_e32 v3, v1
	s_and_saveexec_b64 s[76:77], s[26:27]
	s_cbranch_execz .LBB0_1281
	v_lshrrev_b32_e32 v2, 9, v4
	v_add_u32_e32 v5, 1, v2
	v_and_b32_e32 v4, 0xfffffe, v5
	s_mov_b32 s42, s85
	s_mov_b64 s[24:25], 0
	v_mov_b32_e32 v6, v4
	v_mov_b32_e32 v7, v8
	v_mov_b64_e32 v[2:3], v[202:203]
	v_cmp_ne_u32_e64 s[26:27], 16, v6
	s_cmp_lg_u64 s[26:27], 0
	s_cbranch_scc1 .LBB0_1277
	s_mov_b32 s26, 0x10000
	s_mov_b32 s27, 0
	v_add_u32_e32 v24, s85, v2
	v_add_u32_e32 v22, s42, v3
	v_ashrrev_i32_e32 v25, 31, v24
	v_ashrrev_i32_e32 v23, 31, v22
	v_lshlrev_b64 v[24:25], 6, v[24:25]
	v_lshlrev_b64 v[22:23], 6, v[22:23]
	v_lshl_add_u64 v[24:25], s[48:49], 0, v[24:25]
	v_lshl_add_u64 v[22:23], s[48:49], 0, v[22:23]
	global_load_dword v30, v[24:25], off
	global_load_dword v31, v[22:23], off
	v_lshl_add_u64 v[24:25], v[24:25], 0, s[26:27]
	v_lshl_add_u64 v[22:23], v[22:23], 0, s[26:27]
	global_load_dword v32, v[24:25], off
	global_load_dword v33, v[22:23], off
	v_lshl_add_u64 v[24:25], v[24:25], 0, s[26:27]
	v_lshl_add_u64 v[22:23], v[22:23], 0, s[26:27]
	global_load_dword v34, v[24:25], off
	global_load_dword v35, v[22:23], off
	v_lshl_add_u64 v[24:25], v[24:25], 0, s[26:27]
	v_lshl_add_u64 v[22:23], v[22:23], 0, s[26:27]
	global_load_dword v36, v[24:25], off
	global_load_dword v37, v[22:23], off
	v_lshl_add_u64 v[24:25], v[24:25], 0, s[26:27]
	v_lshl_add_u64 v[22:23], v[22:23], 0, s[26:27]
	global_load_dword v38, v[24:25], off
	global_load_dword v39, v[22:23], off
	v_lshl_add_u64 v[24:25], v[24:25], 0, s[26:27]
	v_lshl_add_u64 v[22:23], v[22:23], 0, s[26:27]
	global_load_dword v40, v[24:25], off
	global_load_dword v41, v[22:23], off
	v_lshl_add_u64 v[24:25], v[24:25], 0, s[26:27]
	v_lshl_add_u64 v[22:23], v[22:23], 0, s[26:27]
	global_load_dword v42, v[24:25], off
	global_load_dword v43, v[22:23], off
	v_lshl_add_u64 v[24:25], v[24:25], 0, s[26:27]
	v_lshl_add_u64 v[22:23], v[22:23], 0, s[26:27]
	global_load_dword v44, v[24:25], off
	global_load_dword v45, v[22:23], off
	s_waitcnt vmcnt(14)
	ds_write2st64_b32 v7, v30, v31 offset1:8
	s_waitcnt vmcnt(12)
	v_add_u32_e32 v7, 0x1000, v7
	ds_write2st64_b32 v7, v32, v33 offset1:8
	s_waitcnt vmcnt(10)
	v_add_u32_e32 v7, 0x1000, v7
	ds_write2st64_b32 v7, v34, v35 offset1:8
	s_waitcnt vmcnt(8)
	v_add_u32_e32 v7, 0x1000, v7
	ds_write2st64_b32 v7, v36, v37 offset1:8
	s_waitcnt vmcnt(6)
	v_add_u32_e32 v7, 0x1000, v7
	ds_write2st64_b32 v7, v38, v39 offset1:8
	s_waitcnt vmcnt(4)
	v_add_u32_e32 v7, 0x1000, v7
	ds_write2st64_b32 v7, v40, v41 offset1:8
	s_waitcnt vmcnt(2)
	v_add_u32_e32 v7, 0x1000, v7
	ds_write2st64_b32 v7, v42, v43 offset1:8
	s_waitcnt vmcnt(0)
	v_add_u32_e32 v7, 0x1000, v7
	ds_write2st64_b32 v7, v44, v45 offset1:8
	s_branch .Lx_tk_done

; __device__ __forceinline__ void topk_phase(Frame& F, KArgs a, int nsets) {
;     ...
;         for (int i = tid; i < n; i += 512) keys[i] = __float_as_uint(AFF[(size_t)(row0 + i) * 16 + e]);
.Lx_tk_done:
	s_or_b64 exec, exec, s[24:25]
	v_cmp_ne_u32_e64 s[26:27], v5, v4
	s_mov_b64 s[24:25], 0
	s_and_saveexec_b64 s[42:43], s[26:27]
	v_lshl_add_u32 v2, v4, 9, v202
	s_mov_b64 s[24:25], exec
	v_lshlrev_b32_e32 v3, 2, v2
	s_or_b64 exec, exec, s[42:43]
	s_orn2_b64 s[24:25], s[24:25], exec

; __device__ __forceinline__ void topk_phase(Frame& F, KArgs a, int nsets) {
;     ...
;         for (int round = 0; round < 4; ++round) {
;             const int shift = 24 - 8 * round;
;             if (tid < 256) hist[tid] = 0u;
;             __syncthreads();
;             const unsigned prefix = misc[0], need = misc[1];
;             for (int i = tid; i < n; i += 512) { const unsigned kk = keys[i]; if (round == 0 || (kk >> (shift + 8)) == prefix) atomicAdd((unsigned*)&hist[(kk >> shift) & 255u], 1u); }
;             __syncthreads();
.LBB0_1289:
	s_and_saveexec_b64 s[24:25], s[6:7]
	ds_write_b32 v8, v195 offset:32768
	s_or_b64 exec, exec, s[24:25]
	s_waitcnt lgkmcnt(0)
	s_barrier
	ds_read_b64 v[2:3], v195 offset:33792
	s_and_saveexec_b64 s[24:25], vcc
	s_cbranch_execz .LBB0_1296
	s_lshl_b32 s26, s42, 3
	s_sub_i32 s43, 24, s26
	s_cmp_eq_u32 s42, 0
	s_cselect_b64 s[28:29], -1, 0
	s_sub_i32 s48, 32, s26
	s_mov_b64 s[30:31], 0
	v_mov_b32_e32 v4, v8
	v_mov_b32_e32 v5, v202
	s_cmpk_lg_i32 s86, 0x2000
	s_cbranch_scc1 .LBB0_1294
	ds_read_b32 v30, v8
	ds_read_b32 v31, v8 offset:2048
	ds_read_b32 v32, v8 offset:4096
	ds_read_b32 v33, v8 offset:6144
	ds_read_b32 v34, v8 offset:8192
	ds_read_b32 v35, v8 offset:10240
	ds_read_b32 v36, v8 offset:12288
	ds_read_b32 v37, v8 offset:14336
	ds_read_b32 v38, v8 offset:16384
	ds_read_b32 v39, v8 offset:18432
	ds_read_b32 v40, v8 offset:20480
	ds_read_b32 v41, v8 offset:22528
	ds_read_b32 v42, v8 offset:24576
	ds_read_b32 v43, v8 offset:26624
	ds_read_b32 v44, v8 offset:28672
	ds_read_b32 v45, v8 offset:30720
	s_waitcnt lgkmcnt(15)
	v_lshrrev_b32_e32 v7, s48, v30
	v_cmp_eq_u32_e64 s[26:27], v7, v2
	s_or_b64 s[52:53], s[28:29], s[26:27]
	s_and_saveexec_b64 s[26:27], s[52:53]
	v_bfe_u32 v6, v30, s43, 8
	v_lshl_add_u32 v6, v6, 2, 0
	ds_add_u32 v6, v224 offset:32768
	s_or_b64 exec, exec, s[26:27]
	s_waitcnt lgkmcnt(14)
	v_lshrrev_b32_e32 v7, s48, v31
	v_cmp_eq_u32_e64 s[26:27], v7, v2
	s_or_b64 s[52:53], s[28:29], s[26:27]
	s_and_saveexec_b64 s[26:27], s[52:53]
	v_bfe_u32 v6, v31, s43, 8
	v_lshl_add_u32 v6, v6, 2, 0
	ds_add_u32 v6, v224 offset:32768
	s_or_b64 exec, exec, s[26:27]
	s_waitcnt lgkmcnt(13)
	v_lshrrev_b32_e32 v7, s48, v32
	v_cmp_eq_u32_e64 s[26:27], v7, v2
	s_or_b64 s[52:53], s[28:29], s[26:27]
	s_and_saveexec_b64 s[26:27], s[52:53]
	v_bfe_u32 v6, v32, s43, 8
	v_lshl_add_u32 v6, v6, 2, 0
	ds_add_u32 v6, v224 offset:32768
	s_or_b64 exec, exec, s[26:27]
	s_waitcnt lgkmcnt(12)
	v_lshrrev_b32_e32 v7, s48, v33
	v_cmp_eq_u32_e64 s[26:27], v7, v2
	s_or_b64 s[52:53], s[28:29], s[26:27]
	s_and_saveexec_b64 s[26:27], s[52:53]
	v_bfe_u32 v6, v33, s43, 8
	v_lshl_add_u32 v6, v6, 2, 0
	ds_add_u32 v6, v224 offset:32768
	s_or_b64 exec, exec, s[26:27]
	s_waitcnt lgkmcnt(11)
	v_lshrrev_b32_e32 v7, s48, v34
	v_cmp_eq_u32_e64 s[26:27], v7, v2
	s_or_b64 s[52:53], s[28:29], s[26:27]
	s_and_saveexec_b64 s[26:27], s[52:53]
	v_bfe_u32 v6, v34, s43, 8
	v_lshl_add_u32 v6, v6, 2, 0
	ds_add_u32 v6, v224 offset:32768
	s_or_b64 exec, exec, s[26:27]
	s_waitcnt lgkmcnt(10)
	v_lshrrev_b32_e32 v7, s48, v35
	v_cmp_eq_u32_e64 s[26:27], v7, v2
	s_or_b64 s[52:53], s[28:29], s[26:27]
	s_and_saveexec_b64 s[26:27], s[52:53]
	v_bfe_u32 v6, v35, s43, 8
	v_lshl_add_u32 v6, v6, 2, 0
	ds_add_u32 v6, v224 offset:32768
	s_or_b64 exec, exec, s[26:27]
	s_waitcnt lgkmcnt(9)
	v_lshrrev_b32_e32 v7, s48, v36
	v_cmp_eq_u32_e64 s[26:27], v7, v2
	s_or_b64 s[52:53], s[28:29], s[26:27]
	s_and_saveexec_b64 s[26:27], s[52:53]
	v_bfe_u32 v6, v36, s43, 8
	v_lshl_add_u32 v6, v6, 2, 0
	ds_add_u32 v6, v224 offset:32768
	s_or_b64 exec, exec, s[26:27]
	s_waitcnt lgkmcnt(8)
	v_lshrrev_b32_e32 v7, s48, v37
	v_cmp_eq_u32_e64 s[26:27], v7, v2
	s_or_b64 s[52:53], s[28:29], s[26:27]
	s_and_saveexec_b64 s[26:27], s[52:53]
	v_bfe_u32 v6, v37, s43, 8
	v_lshl_add_u32 v6, v6, 2, 0
	ds_add_u32 v6, v224 offset:32768
	s_or_b64 exec, exec, s[26:27]
	s_waitcnt lgkmcnt(7)
	v_lshrrev_b32_e32 v7, s48, v38
	v_cmp_eq_u32_e64 s[26:27], v7, v2
	s_or_b64 s[52:53], s[28:29], s[26:27]
	s_and_saveexec_b64 s[26:27], s[52:53]
	v_bfe_u32 v6, v38, s43, 8
	v_lshl_add_u32 v6, v6, 2, 0
	ds_add_u32 v6, v224 offset:32768
	s_or_b64 exec, exec, s[26:27]
	s_waitcnt lgkmcnt(6)
	v_lshrrev_b32_e32 v7, s48, v39
	v_cmp_eq_u32_e64 s[26:27], v7, v2
	s_or_b64 s[52:53], s[28:29], s[26:27]
	s_and_saveexec_b64 s[26:27], s[52:53]
	v_bfe_u32 v6, v39, s43, 8
	v_lshl_add_u32 v6, v6, 2, 0
	ds_add_u32 v6, v224 offset:32768
	s_or_b64 exec, exec, s[26:27]
	s_waitcnt lgkmcnt(5)
	v_lshrrev_b32_e32 v7, s48, v40
	v_cmp_eq_u32_e64 s[26:27], v7, v2
	s_or_b64 s[52:53], s[28:29], s[26:27]
	s_and_saveexec_b64 s[26:27], s[52:53]
	v_bfe_u32 v6, v40, s43, 8
	v_lshl_add_u32 v6, v6, 2, 0
	ds_add_u32 v6, v224 offset:32768
	s_or_b64 exec, exec, s[26:27]
	s_waitcnt lgkmcnt(4)
	v_lshrrev_b32_e32 v7, s48, v41
	v_cmp_eq_u32_e64 s[26:27], v7, v2
	s_or_b64 s[52:53], s[28:29], s[26:27]
	s_and_saveexec_b64 s[26:27], s[52:53]
	v_bfe_u32 v6, v41, s43, 8
	v_lshl_add_u32 v6, v6, 2, 0
	ds_add_u32 v6, v224 offset:32768
	s_or_b64 exec, exec, s[26:27]
	s_waitcnt lgkmcnt(3)
	v_lshrrev_b32_e32 v7, s48, v42
	v_cmp_eq_u32_e64 s[26:27], v7, v2
	s_or_b64 s[52:53], s[28:29], s[26:27]
	s_and_saveexec_b64 s[26:27], s[52:53]
	v_bfe_u32 v6, v42, s43, 8
	v_lshl_add_u32 v6, v6, 2, 0
	ds_add_u32 v6, v224 offset:32768
	s_or_b64 exec, exec, s[26:27]
	s_waitcnt lgkmcnt(2)
	v_lshrrev_b32_e32 v7, s48, v43
	v_cmp_eq_u32_e64 s[26:27], v7, v2
	s_or_b64 s[52:53], s[28:29], s[26:27]
	s_and_saveexec_b64 s[26:27], s[52:53]
	v_bfe_u32 v6, v43, s43, 8
	v_lshl_add_u32 v6, v6, 2, 0
	ds_add_u32 v6, v224 offset:32768
	s_or_b64 exec, exec, s[26:27]
	s_waitcnt lgkmcnt(1)
	v_lshrrev_b32_e32 v7, s48, v44
	v_cmp_eq_u32_e64 s[26:27], v7, v2
	s_or_b64 s[52:53], s[28:29], s[26:27]
	s_and_saveexec_b64 s[26:27], s[52:53]
	v_bfe_u32 v6, v44, s43, 8
	v_lshl_add_u32 v6, v6, 2, 0
	ds_add_u32 v6, v224 offset:32768
	s_or_b64 exec, exec, s[26:27]
	s_waitcnt lgkmcnt(0)
	v_lshrrev_b32_e32 v7, s48, v45
	v_cmp_eq_u32_e64 s[26:27], v7, v2
	s_or_b64 s[52:53], s[28:29], s[26:27]
	s_and_saveexec_b64 s[26:27], s[52:53]
	v_bfe_u32 v6, v45, s43, 8
	v_lshl_add_u32 v6, v6, 2, 0
	ds_add_u32 v6, v224 offset:32768
	s_or_b64 exec, exec, s[26:27]
	s_branch .LBB0_1296
